# P10: each wave owns 64 contiguous output columns; a unit's e4m3 results are packed into a register buffer and stored one row group per K-iteration of the NEXT unit (trickled under the MFMAs) instead o
# speedup vs baseline: 1.0341x; 1.0094x over previous
.LBB0_1432:
	s_add_u32 s18, s6, 0x44000000
	s_addc_u32 s19, s7, 0
	s_lshl_b32 s6, s20, 5
	s_and_b32 s9, s6, 0x60
	s_lshr_b32 s6, s94, 29
	v_readlane_b32 s7, v255, 19
	s_mov_b64 s[20:21], 0x80
	s_add_i32 s6, s7, s6
	v_lshl_add_u64 v[8:9], v[8:9], 0, s[20:21]
	s_add_i32 m0, s1, 0x18000
	s_lshl_b32 s8, s23, 13
	s_lshl_b32 s11, s9, 8
	s_ashr_i32 s59, s6, 3
	s_waitcnt vmcnt(2)
	s_barrier
	global_load_lds_dwordx4 v[8:9], off
	v_lshl_add_u64 v[4:5], v[4:5], 0, s[20:21]
	s_add_i32 m0, s1, 0x1a000
	s_add_i32 s60, s1, 0x8000
	s_add_i32 s61, s1, 0xa000
	global_load_lds_dwordx4 v[4:5], off
	v_lshl_add_u64 v[2:3], v[2:3], 0, s[20:21]
	s_mov_b32 m0, s60
	s_add_u32 s6, s44, 0x40080
	global_load_lds_dwordx4 v[2:3], off
	v_lshl_add_u64 v[2:3], v[6:7], 0, s[20:21]
	s_mov_b32 m0, s61
	s_addc_u32 s7, s45, 0
	global_load_lds_dwordx4 v[2:3], off
	v_lshl_add_u64 v[2:3], s[6:7], 0, v[164:165]
	s_add_i32 m0, s1, 0x1c000
	v_mov_b32_e32 v171, v165
	global_load_lds_dwordx4 v[2:3], off
	v_lshl_add_u64 v[2:3], s[6:7], 0, v[162:163]
	s_add_i32 m0, s1, 0x1e000
	s_cmpk_lt_u32 s22, 0x100
	global_load_lds_dwordx4 v[2:3], off
	v_lshrrev_b32_e32 v3, 1, v10
	v_and_b32_e32 v3, 24, v3
	v_and_b32_e32 v2, 15, v10
	v_lshlrev_b32_e32 v4, 1, v3
	v_lshl_or_b32 v1, s23, 6, v2
	v_lshl_or_b32 v2, v2, 6, v4
	v_lshlrev_b32_e32 v4, 2, v10
	v_and_b32_e32 v4, 32, v4
	s_waitcnt vmcnt(6)
	v_bitop3_b32 v5, v2, s8, v4 bitop3:0xde
	v_bitop3_b32 v182, v2, s11, v4 bitop3:0xde
	s_cselect_b64 s[22:23], -1, 0
	s_add_i32 s6, 0, 0x210c0
	s_add_i32 s80, 0, 0x10000
	s_add_i32 s81, 0, 0x14000
	v_mov_b32_e32 v173, v165
	s_mov_b32 s62, 0
	v_lshl_or_b32 v183, s9, 1, v3
	v_mov_b32_e32 v184, s6
	s_add_i32 s63, 0, 0x21044
	s_add_i32 s64, 0, 0x2104c
	s_add_i32 s65, 0, 0x21054
	s_add_i32 s66, 0, 0x2105c
	s_add_i32 s67, 0, 0x21064
	s_add_i32 s68, 0, 0x2106c
	s_add_i32 s69, 0, 0x21074
	s_add_i32 s70, 0, 0x2107c
	s_add_i32 s71, 0, 0x21084
	s_add_i32 s72, 0, 0x2108c
	s_add_i32 s73, 0, 0x21094
	s_add_i32 s75, 0, 0x2109c
	s_add_i32 s76, 0, 0x210a4
	s_add_i32 s77, 0, 0x210ac
	s_add_i32 s78, 0, 0x210b4
	s_add_i32 s79, 0, 0x210bc
	v_add_u32_e32 v185, s80, v182
	v_add_u32_e32 v186, 0x1000, v185
	v_add_u32_e32 v187, 0, v5
	s_mov_b64 s[24:25], 0x48000
	s_mov_b64 s[26:27], 0x50000
	s_mov_b64 s[28:29], 0x58000
	s_mov_b32 s30, 0x3d000000
	s_mov_b32 s82, 0x48000
	s_mov_b32 s83, 0x50000
	s_mov_b32 s84, 0x58000
	s_mov_b32 s85, s0
	v_mbcnt_lo_u32_b32 v250, -1, 0
	v_mbcnt_hi_u32_b32 v250, -1, v250
	v_mul_u32_u24_e32 v250, s59, v250
	v_add_u32_e32 v250, s98, v250
	v_sub_u32_e32 v250, s99, v250
	v_add_u32_e32 v250, -1, v250
	v_mov_b32_e32 v251, 0x21040
	ds_read_b32 v34, v251 offset:4
	ds_read_b32 v35, v251 offset:8
	ds_read_b32 v36, v251 offset:12
	ds_read_b32 v37, v251 offset:16
	ds_read_b32 v38, v251 offset:20
	ds_read_b32 v39, v251 offset:24
	ds_read_b32 v40, v251 offset:28
	ds_read_b32 v41, v251 offset:32
	ds_read_b32 v42, v251 offset:36
	ds_read_b32 v43, v251 offset:40
	ds_read_b32 v44, v251 offset:44
	ds_read_b32 v45, v251 offset:48
	ds_read_b32 v46, v251 offset:52
	ds_read_b32 v47, v251 offset:56
	ds_read_b32 v48, v251 offset:60
	ds_read_b32 v49, v251 offset:64
	ds_read_b32 v50, v251 offset:68
	ds_read_b32 v51, v251 offset:72
	ds_read_b32 v52, v251 offset:76
	ds_read_b32 v53, v251 offset:80
	ds_read_b32 v54, v251 offset:84
	ds_read_b32 v55, v251 offset:88
	ds_read_b32 v56, v251 offset:92
	ds_read_b32 v57, v251 offset:96
	ds_read_b32 v58, v251 offset:100
	ds_read_b32 v59, v251 offset:104
	ds_read_b32 v60, v251 offset:108
	ds_read_b32 v61, v251 offset:112
	ds_read_b32 v62, v251 offset:116
	ds_read_b32 v63, v251 offset:120
	ds_read_b32 v64, v251 offset:124
	ds_read_b32 v65, v251 offset:128
	v_mov_b32_e32 v254, 0
	s_waitcnt lgkmcnt(0)
	v_cmp_ge_i32_e32 vcc, v250, v34
	s_nop 1
	v_addc_co_u32_e32 v254, vcc, 0, v254, vcc
	v_cmp_ge_i32_e32 vcc, v250, v35
	s_nop 1
	v_addc_co_u32_e32 v254, vcc, 0, v254, vcc
	v_cmp_ge_i32_e32 vcc, v250, v36
	s_nop 1
	v_addc_co_u32_e32 v254, vcc, 0, v254, vcc
	v_cmp_ge_i32_e32 vcc, v250, v37
	s_nop 1
	v_addc_co_u32_e32 v254, vcc, 0, v254, vcc
	v_cmp_ge_i32_e32 vcc, v250, v38
	s_nop 1
	v_addc_co_u32_e32 v254, vcc, 0, v254, vcc
	v_cmp_ge_i32_e32 vcc, v250, v39
	s_nop 1
	v_addc_co_u32_e32 v254, vcc, 0, v254, vcc
	v_cmp_ge_i32_e32 vcc, v250, v40
	s_nop 1
	v_addc_co_u32_e32 v254, vcc, 0, v254, vcc
	v_cmp_ge_i32_e32 vcc, v250, v41
	s_nop 1
	v_addc_co_u32_e32 v254, vcc, 0, v254, vcc
	v_cmp_ge_i32_e32 vcc, v250, v42
	s_nop 1
	v_addc_co_u32_e32 v254, vcc, 0, v254, vcc
	v_cmp_ge_i32_e32 vcc, v250, v43
	s_nop 1
	v_addc_co_u32_e32 v254, vcc, 0, v254, vcc
	v_cmp_ge_i32_e32 vcc, v250, v44
	s_nop 1
	v_addc_co_u32_e32 v254, vcc, 0, v254, vcc
	v_cmp_ge_i32_e32 vcc, v250, v45
	s_nop 1
	v_addc_co_u32_e32 v254, vcc, 0, v254, vcc
	v_cmp_ge_i32_e32 vcc, v250, v46
	s_nop 1
	v_addc_co_u32_e32 v254, vcc, 0, v254, vcc
	v_cmp_ge_i32_e32 vcc, v250, v47
	s_nop 1
	v_addc_co_u32_e32 v254, vcc, 0, v254, vcc
	v_cmp_ge_i32_e32 vcc, v250, v48
	s_nop 1
	v_addc_co_u32_e32 v254, vcc, 0, v254, vcc
	v_cmp_ge_i32_e32 vcc, v250, v49
	s_nop 1
	v_addc_co_u32_e32 v254, vcc, 0, v254, vcc
	v_cmp_ge_i32_e32 vcc, v250, v50
	s_nop 1
	v_addc_co_u32_e32 v254, vcc, 0, v254, vcc
	v_cmp_ge_i32_e32 vcc, v250, v51
	s_nop 1
	v_addc_co_u32_e32 v254, vcc, 0, v254, vcc
	v_cmp_ge_i32_e32 vcc, v250, v52
	s_nop 1
	v_addc_co_u32_e32 v254, vcc, 0, v254, vcc
	v_cmp_ge_i32_e32 vcc, v250, v53
	s_nop 1
	v_addc_co_u32_e32 v254, vcc, 0, v254, vcc
	v_cmp_ge_i32_e32 vcc, v250, v54
	s_nop 1
	v_addc_co_u32_e32 v254, vcc, 0, v254, vcc
	v_cmp_ge_i32_e32 vcc, v250, v55
	s_nop 1
	v_addc_co_u32_e32 v254, vcc, 0, v254, vcc
	v_cmp_ge_i32_e32 vcc, v250, v56
	s_nop 1
	v_addc_co_u32_e32 v254, vcc, 0, v254, vcc
	v_cmp_ge_i32_e32 vcc, v250, v57
	s_nop 1
	v_addc_co_u32_e32 v254, vcc, 0, v254, vcc
	v_cmp_ge_i32_e32 vcc, v250, v58
	s_nop 1
	v_addc_co_u32_e32 v254, vcc, 0, v254, vcc
	v_cmp_ge_i32_e32 vcc, v250, v59
	s_nop 1
	v_addc_co_u32_e32 v254, vcc, 0, v254, vcc
	v_cmp_ge_i32_e32 vcc, v250, v60
	s_nop 1
	v_addc_co_u32_e32 v254, vcc, 0, v254, vcc
	v_cmp_ge_i32_e32 vcc, v250, v61
	s_nop 1
	v_addc_co_u32_e32 v254, vcc, 0, v254, vcc
	v_cmp_ge_i32_e32 vcc, v250, v62
	s_nop 1
	v_addc_co_u32_e32 v254, vcc, 0, v254, vcc
	v_cmp_ge_i32_e32 vcc, v250, v63
	s_nop 1
	v_addc_co_u32_e32 v254, vcc, 0, v254, vcc
	v_cmp_ge_i32_e32 vcc, v250, v64
	s_nop 1
	v_addc_co_u32_e32 v254, vcc, 0, v254, vcc
	v_bfe_u32 v250, v183, 3, 1
	v_mul_u32_u24_e32 v250, 24, v250
	v_add_u32_e32 v250, v250, v183
	v_lshl_add_u32 v1, v1, 11, v250
	s_mov_b32 s100, s85
	s_mov_b32 s101, 0
	s_lshl_b64 s[100:101], s[100:101], 19
	s_add_u32 s100, s100, s18
	s_addc_u32 s101, s101, s19
	s_lshl_b32 vcc_lo, s10, 8
	s_add_u32 s100, s100, vcc_lo
	s_addc_u32 s101, s101, 0
	s_barrier
	s_branch .LBB0_1435

.LBB0_1439:
	s_ashr_i32 s37, s36, 31
	s_lshl_b64 s[38:39], s[36:37], 19
	s_add_u32 s38, s31, s38
	s_addc_u32 s39, s52, s39
	s_add_u32 s35, s42, 0x100
	s_addc_u32 s11, s43, 0
	s_and_b64 s[46:47], s[6:7], exec
	s_cselect_b32 s11, s39, s11
	s_cselect_b32 s35, s38, s35
	s_mov_b32 s37, -2
	ds_read_b128 v[18:21], v185
	ds_read_b128 v[22:25], v185 offset:1024
	ds_read_b128 v[26:29], v185 offset:2048
	ds_read_b128 v[30:33], v185 offset:3072
	ds_read_b128 v[2:5], v186
	ds_read_b128 v[6:9], v186 offset:1024
	ds_read_b128 v[10:13], v186 offset:2048
	ds_read_b128 v[14:17], v186 offset:3072
	s_add_u32 s50, s42, 0x80
	s_addc_u32 s51, s43, 0
	s_add_u32 s42, s42, 0x100
	s_addc_u32 s43, s43, 0
	s_add_u32 s44, s44, 0x100
	s_addc_u32 s45, s45, 0
	s_cmp_eq_u32 s37, 12
	s_cselect_b32 s48, s35, s42
	s_cselect_b32 s49, s11, s43
	s_cselect_b32 s46, s8, s44
	s_cselect_b32 s47, s9, s45
	v_lshl_add_u64 v[212:213], s[50:51], 0, v[170:171]
	s_add_i32 m0, s1, 0xc000
	ds_read_b128 v[174:177], v187
	ds_read_b128 v[178:181], v187 offset:1024
	ds_read_b128 v[188:191], v187 offset:2048
	ds_read_b128 v[192:195], v187 offset:3072
	ds_read_b128 v[196:199], v187 offset:4096
	ds_read_b128 v[200:203], v187 offset:5120
	ds_read_b128 v[204:207], v187 offset:6144
	ds_read_b128 v[208:211], v187 offset:7168
	global_load_lds_dwordx4 v[212:213], off
	v_lshl_add_u64 v[212:213], s[50:51], 0, v[172:173]
	s_add_i32 m0, s1, 0xe000
	s_nop 0
	global_load_lds_dwordx4 v[212:213], off
	global_store_dwordx4 v1, v[222:225], s[100:101]
	s_mov_b32 vcc_lo, 0x8000
	s_cmp_eq_u32 s37, 4
	s_cselect_b32 vcc_lo, 0x28000, vcc_lo
	s_add_u32 s100, s100, vcc_lo
	s_addc_u32 s101, s101, 0
	v_mov_b32_e32 v222, v226
	v_mov_b32_e32 v223, v227
	v_mov_b32_e32 v224, v228
	v_mov_b32_e32 v225, v229
	v_mov_b32_e32 v226, v230
	v_mov_b32_e32 v227, v231
	v_mov_b32_e32 v228, v232
	v_mov_b32_e32 v229, v233
	v_mov_b32_e32 v230, v234
	v_mov_b32_e32 v231, v235
	v_mov_b32_e32 v232, v236
	v_mov_b32_e32 v233, v237
	v_mov_b32_e32 v234, v238
	v_mov_b32_e32 v235, v239
	v_mov_b32_e32 v236, v240
	v_mov_b32_e32 v237, v241
	v_mov_b32_e32 v238, v242
	v_mov_b32_e32 v239, v243
	v_mov_b32_e32 v240, v244
	v_mov_b32_e32 v241, v245
	v_mov_b32_e32 v242, v246
	v_mov_b32_e32 v243, v247
	v_mov_b32_e32 v244, v248
	v_mov_b32_e32 v245, v249
	v_mov_b32_e32 v246, v250
	v_mov_b32_e32 v247, v251
	v_mov_b32_e32 v248, v252
	v_mov_b32_e32 v249, v253
	s_waitcnt vmcnt(9)
	s_waitcnt lgkmcnt(0)
	s_barrier
	s_setprio 1
	s_waitcnt lgkmcnt(0)
	v_mfma_f32_16x16x128_f8f6f4 v[158:161], v[18:25], v[174:181], 0
	v_mfma_f32_16x16x128_f8f6f4 v[154:157], v[26:33], v[174:181], 0
	v_mfma_f32_16x16x128_f8f6f4 v[150:153], v[18:25], v[188:195], 0
	v_mfma_f32_16x16x128_f8f6f4 v[146:149], v[26:33], v[188:195], 0
	v_mfma_f32_16x16x128_f8f6f4 v[142:145], v[18:25], v[196:203], 0
	v_mfma_f32_16x16x128_f8f6f4 v[134:137], v[26:33], v[196:203], 0
	v_mfma_f32_16x16x128_f8f6f4 v[118:121], v[18:25], v[204:211], 0
	v_mfma_f32_16x16x128_f8f6f4 v[110:113], v[26:33], v[204:211], 0
	s_setprio 0
	s_setprio 1
	v_mfma_f32_16x16x128_f8f6f4 v[138:141], v[2:9], v[174:181], 0
	v_mfma_f32_16x16x128_f8f6f4 v[130:133], v[10:17], v[174:181], 0
	v_mfma_f32_16x16x128_f8f6f4 v[126:129], v[2:9], v[188:195], 0
	v_mfma_f32_16x16x128_f8f6f4 v[122:125], v[10:17], v[188:195], 0
	v_mfma_f32_16x16x128_f8f6f4 v[114:117], v[2:9], v[196:203], 0
	v_mfma_f32_16x16x128_f8f6f4 v[106:109], v[10:17], v[196:203], 0
	v_mfma_f32_16x16x128_f8f6f4 v[102:105], v[2:9], v[204:211], 0
	v_mfma_f32_16x16x128_f8f6f4 v[98:101], v[10:17], v[204:211], 0
	s_setprio 0
	s_barrier
	s_add_i32 s41, s80, s56
	v_lshl_add_u64 v[174:175], s[46:47], 0, v[164:165]
	s_mov_b32 m0, s41
	ds_read_b128 v[188:191], v187 offset:16384
	ds_read_b128 v[192:195], v187 offset:17408
	ds_read_b128 v[196:199], v187 offset:18432
	ds_read_b128 v[200:203], v187 offset:19456
	ds_read_b128 v[204:207], v187 offset:20480
	ds_read_b128 v[208:211], v187 offset:21504
	ds_read_b128 v[212:215], v187 offset:22528
	ds_read_b128 v[216:219], v187 offset:23552
	global_load_lds_dwordx4 v[174:175], off
	s_add_i32 m0, s41, 0x2000
	s_add_u32 s50, s46, 0x40000
	v_lshl_add_u64 v[176:177], s[46:47], 0, v[162:163]
	s_addc_u32 s51, s47, 0
	s_add_i32 s41, s81, s56
	global_load_lds_dwordx4 v[176:177], off
	v_lshl_add_u64 v[178:179], s[50:51], 0, v[164:165]
	s_mov_b32 m0, s41
	v_lshl_add_u64 v[180:181], s[48:49], 0, v[168:169]
	global_load_lds_dwordx4 v[178:179], off
	v_lshl_add_u64 v[178:179], s[50:51], 0, v[162:163]
	s_add_i32 m0, s41, 0x2000
	s_nop 0
	global_load_lds_dwordx4 v[178:179], off
	v_lshl_add_u64 v[178:179], s[48:49], 0, v[166:167]
	s_mov_b32 m0, s1
	s_nop 0
	global_load_lds_dwordx4 v[178:179], off
	s_mov_b32 m0, s33
	s_nop 0
	global_load_lds_dwordx4 v[180:181], off
	s_waitcnt vmcnt(9)
	s_waitcnt lgkmcnt(0)
	s_barrier
	s_setprio 1
	s_waitcnt lgkmcnt(0)
	v_mfma_f32_16x16x128_f8f6f4 v[94:97], v[18:25], v[188:195], 0
	v_mfma_f32_16x16x128_f8f6f4 v[90:93], v[26:33], v[188:195], 0
	v_mfma_f32_16x16x128_f8f6f4 v[78:81], v[18:25], v[196:203], 0
	v_mfma_f32_16x16x128_f8f6f4 v[66:69], v[26:33], v[196:203], 0
	v_mfma_f32_16x16x128_f8f6f4 v[50:53], v[18:25], v[204:211], 0
	v_mfma_f32_16x16x128_f8f6f4 v[46:49], v[26:33], v[204:211], 0
	v_mfma_f32_16x16x128_f8f6f4 v[38:41], v[18:25], v[212:219], 0
	v_mfma_f32_16x16x128_f8f6f4 v[34:37], v[26:33], v[212:219], 0
	s_setprio 0
	s_setprio 1
	v_mfma_f32_16x16x128_f8f6f4 v[82:85], v[2:9], v[188:195], 0
	v_mfma_f32_16x16x128_f8f6f4 v[70:73], v[10:17], v[188:195], 0
	v_mfma_f32_16x16x128_f8f6f4 v[54:57], v[2:9], v[196:203], 0
	v_mfma_f32_16x16x128_f8f6f4 v[42:45], v[10:17], v[196:203], 0
	v_mfma_f32_16x16x128_f8f6f4 v[74:77], v[2:9], v[204:211], 0
	v_mfma_f32_16x16x128_f8f6f4 v[86:89], v[10:17], v[204:211], 0
	v_mfma_f32_16x16x128_f8f6f4 v[58:61], v[2:9], v[212:219], 0
	v_mfma_f32_16x16x128_f8f6f4 v[62:65], v[10:17], v[212:219], 0
	s_setprio 0
	s_barrier
	s_add_i32 s41, 0, 0x18000
	s_add_i32 s50, 0, 0x1c000
	v_add_u32_e32 v14, s41, v182
	v_add_u32_e32 v30, 0x1000, v14
	ds_read_b128 v[2:5], v14
	ds_read_b128 v[6:9], v14 offset:1024
	ds_read_b128 v[10:13], v14 offset:2048
	ds_read_b128 v[14:17], v14 offset:3072
	ds_read_b128 v[18:21], v30
	ds_read_b128 v[22:25], v30 offset:1024
	ds_read_b128 v[26:29], v30 offset:2048
	ds_read_b128 v[30:33], v30 offset:3072
	s_mov_b32 m0, s54
	v_lshl_add_u64 v[220:221], s[48:49], 0, v[170:171]
	ds_read_b128 v[188:191], v187 offset:32768
	ds_read_b128 v[192:195], v187 offset:33792
	ds_read_b128 v[196:199], v187 offset:34816
	ds_read_b128 v[200:203], v187 offset:35840
	ds_read_b128 v[204:207], v187 offset:36864
	ds_read_b128 v[208:211], v187 offset:37888
	ds_read_b128 v[212:215], v187 offset:38912
	ds_read_b128 v[216:219], v187 offset:39936
	global_load_lds_dwordx4 v[220:221], off
	v_lshl_add_u64 v[220:221], s[48:49], 0, v[172:173]
	s_mov_b32 m0, s57
	s_nop 0
	global_load_lds_dwordx4 v[220:221], off
	s_waitcnt vmcnt(9)
	s_waitcnt lgkmcnt(0)
	s_barrier
	s_setprio 1
	s_waitcnt lgkmcnt(0)
	v_mfma_f32_16x16x128_f8f6f4 v[158:161], v[2:9], v[188:195], v[158:161]
	v_mfma_f32_16x16x128_f8f6f4 v[154:157], v[10:17], v[188:195], v[154:157]
	v_mfma_f32_16x16x128_f8f6f4 v[150:153], v[2:9], v[196:203], v[150:153]
	v_mfma_f32_16x16x128_f8f6f4 v[146:149], v[10:17], v[196:203], v[146:149]
	v_mfma_f32_16x16x128_f8f6f4 v[142:145], v[2:9], v[204:211], v[142:145]
	v_mfma_f32_16x16x128_f8f6f4 v[134:137], v[10:17], v[204:211], v[134:137]
	v_mfma_f32_16x16x128_f8f6f4 v[118:121], v[2:9], v[212:219], v[118:121]
	v_mfma_f32_16x16x128_f8f6f4 v[110:113], v[10:17], v[212:219], v[110:113]
	s_setprio 0
	s_setprio 1
	v_mfma_f32_16x16x128_f8f6f4 v[138:141], v[18:25], v[188:195], v[138:141]
	v_mfma_f32_16x16x128_f8f6f4 v[130:133], v[26:33], v[188:195], v[130:133]
	v_mfma_f32_16x16x128_f8f6f4 v[126:129], v[18:25], v[196:203], v[126:129]
	v_mfma_f32_16x16x128_f8f6f4 v[122:125], v[26:33], v[196:203], v[122:125]
	v_mfma_f32_16x16x128_f8f6f4 v[114:117], v[18:25], v[204:211], v[114:117]
	v_mfma_f32_16x16x128_f8f6f4 v[106:109], v[26:33], v[204:211], v[106:109]
	v_mfma_f32_16x16x128_f8f6f4 v[102:105], v[18:25], v[212:219], v[102:105]
	v_mfma_f32_16x16x128_f8f6f4 v[98:101], v[26:33], v[212:219], v[98:101]
	s_setprio 0
	s_barrier
	s_add_i32 s41, s41, s56
	v_lshl_add_u64 v[174:175], v[174:175], 0, s[20:21]
	s_mov_b32 m0, s41
	ds_read_b128 v[188:191], v187 offset:49152
	ds_read_b128 v[192:195], v187 offset:50176
	ds_read_b128 v[196:199], v187 offset:51200
	ds_read_b128 v[200:203], v187 offset:52224
	ds_read_b128 v[204:207], v187 offset:53248
	ds_read_b128 v[208:211], v187 offset:54272
	ds_read_b128 v[212:215], v187 offset:55296
	ds_read_b128 v[216:219], v187 offset:56320
	global_load_lds_dwordx4 v[174:175], off
	s_add_i32 m0, s41, 0x2000
	s_add_u32 s46, s46, 0x40080
	v_lshl_add_u64 v[174:175], v[176:177], 0, s[20:21]
	s_addc_u32 s47, s47, 0
	s_add_i32 s41, s50, s56
	global_load_lds_dwordx4 v[174:175], off
	v_lshl_add_u64 v[174:175], s[46:47], 0, v[164:165]
	s_mov_b32 m0, s41
	s_nop 0
	global_load_lds_dwordx4 v[174:175], off
	v_lshl_add_u64 v[174:175], s[46:47], 0, v[162:163]
	s_add_i32 m0, s41, 0x2000
	s_nop 0
	global_load_lds_dwordx4 v[174:175], off
	v_lshl_add_u64 v[174:175], v[178:179], 0, s[20:21]
	s_mov_b32 m0, s60
	s_nop 0
	global_load_lds_dwordx4 v[174:175], off
	v_lshl_add_u64 v[174:175], v[180:181], 0, s[20:21]
	s_mov_b32 m0, s61
	s_nop 0
	global_load_lds_dwordx4 v[174:175], off
	s_waitcnt vmcnt(8)
	s_waitcnt lgkmcnt(0)
	s_barrier
	s_setprio 1
	s_waitcnt lgkmcnt(0)
	v_mfma_f32_16x16x128_f8f6f4 v[94:97], v[2:9], v[188:195], v[94:97]
	v_mfma_f32_16x16x128_f8f6f4 v[90:93], v[10:17], v[188:195], v[90:93]
	v_mfma_f32_16x16x128_f8f6f4 v[78:81], v[2:9], v[196:203], v[78:81]
	v_mfma_f32_16x16x128_f8f6f4 v[66:69], v[10:17], v[196:203], v[66:69]
	v_mfma_f32_16x16x128_f8f6f4 v[50:53], v[2:9], v[204:211], v[50:53]
	v_mfma_f32_16x16x128_f8f6f4 v[46:49], v[10:17], v[204:211], v[46:49]
	v_mfma_f32_16x16x128_f8f6f4 v[38:41], v[2:9], v[212:219], v[38:41]
	v_mfma_f32_16x16x128_f8f6f4 v[34:37], v[10:17], v[212:219], v[34:37]
	s_setprio 0
	s_setprio 1
	v_mfma_f32_16x16x128_f8f6f4 v[82:85], v[18:25], v[188:195], v[82:85]
	v_mfma_f32_16x16x128_f8f6f4 v[70:73], v[26:33], v[188:195], v[70:73]
	v_mfma_f32_16x16x128_f8f6f4 v[54:57], v[18:25], v[196:203], v[54:57]
	v_mfma_f32_16x16x128_f8f6f4 v[42:45], v[26:33], v[196:203], v[42:45]
	v_mfma_f32_16x16x128_f8f6f4 v[74:77], v[18:25], v[204:211], v[74:77]
	v_mfma_f32_16x16x128_f8f6f4 v[86:89], v[26:33], v[204:211], v[86:89]
	v_mfma_f32_16x16x128_f8f6f4 v[58:61], v[18:25], v[212:219], v[58:61]
	v_mfma_f32_16x16x128_f8f6f4 v[62:65], v[26:33], v[212:219], v[62:65]
	s_setprio 0
	s_barrier
	s_add_i32 s37, s37, 2
.LBB0_1440:
	ds_read_b128 v[18:21], v185
	ds_read_b128 v[22:25], v185 offset:1024
	ds_read_b128 v[26:29], v185 offset:2048
	ds_read_b128 v[30:33], v185 offset:3072
	ds_read_b128 v[2:5], v186
	ds_read_b128 v[6:9], v186 offset:1024
	ds_read_b128 v[10:13], v186 offset:2048
	ds_read_b128 v[14:17], v186 offset:3072
	s_add_u32 s50, s42, 0x80
	s_addc_u32 s51, s43, 0
	s_add_u32 s42, s42, 0x100
	s_addc_u32 s43, s43, 0
	s_add_u32 s44, s44, 0x100
	s_addc_u32 s45, s45, 0
	s_cmp_eq_u32 s37, 12
	s_cselect_b32 s48, s35, s42
	s_cselect_b32 s49, s11, s43
	s_cselect_b32 s46, s8, s44
	s_cselect_b32 s47, s9, s45
	v_lshl_add_u64 v[212:213], s[50:51], 0, v[170:171]
	s_add_i32 m0, s1, 0xc000
	ds_read_b128 v[174:177], v187
	ds_read_b128 v[178:181], v187 offset:1024
	ds_read_b128 v[188:191], v187 offset:2048
	ds_read_b128 v[192:195], v187 offset:3072
	ds_read_b128 v[196:199], v187 offset:4096
	ds_read_b128 v[200:203], v187 offset:5120
	ds_read_b128 v[204:207], v187 offset:6144
	ds_read_b128 v[208:211], v187 offset:7168
	global_load_lds_dwordx4 v[212:213], off
	v_lshl_add_u64 v[212:213], s[50:51], 0, v[172:173]
	s_add_i32 m0, s1, 0xe000
	s_nop 0
	global_load_lds_dwordx4 v[212:213], off
	global_store_dwordx4 v1, v[222:225], s[100:101]
	s_mov_b32 vcc_lo, 0x8000
	s_cmp_eq_u32 s37, 4
	s_cselect_b32 vcc_lo, 0x28000, vcc_lo
	s_add_u32 s100, s100, vcc_lo
	s_addc_u32 s101, s101, 0
	v_mov_b32_e32 v222, v226
	v_mov_b32_e32 v223, v227
	v_mov_b32_e32 v224, v228
	v_mov_b32_e32 v225, v229
	v_mov_b32_e32 v226, v230
	v_mov_b32_e32 v227, v231
	v_mov_b32_e32 v228, v232
	v_mov_b32_e32 v229, v233
	v_mov_b32_e32 v230, v234
	v_mov_b32_e32 v231, v235
	v_mov_b32_e32 v232, v236
	v_mov_b32_e32 v233, v237
	v_mov_b32_e32 v234, v238
	v_mov_b32_e32 v235, v239
	v_mov_b32_e32 v236, v240
	v_mov_b32_e32 v237, v241
	v_mov_b32_e32 v238, v242
	v_mov_b32_e32 v239, v243
	v_mov_b32_e32 v240, v244
	v_mov_b32_e32 v241, v245
	v_mov_b32_e32 v242, v246
	v_mov_b32_e32 v243, v247
	v_mov_b32_e32 v244, v248
	v_mov_b32_e32 v245, v249
	v_mov_b32_e32 v246, v250
	v_mov_b32_e32 v247, v251
	v_mov_b32_e32 v248, v252
	v_mov_b32_e32 v249, v253
	s_waitcnt vmcnt(9)
	s_waitcnt lgkmcnt(0)
	s_barrier
	s_setprio 1
	s_waitcnt lgkmcnt(0)
	v_mfma_f32_16x16x128_f8f6f4 v[158:161], v[18:25], v[174:181], v[158:161]
	v_mfma_f32_16x16x128_f8f6f4 v[154:157], v[26:33], v[174:181], v[154:157]
	v_mfma_f32_16x16x128_f8f6f4 v[150:153], v[18:25], v[188:195], v[150:153]
	v_mfma_f32_16x16x128_f8f6f4 v[146:149], v[26:33], v[188:195], v[146:149]
	v_mfma_f32_16x16x128_f8f6f4 v[142:145], v[18:25], v[196:203], v[142:145]
	v_mfma_f32_16x16x128_f8f6f4 v[134:137], v[26:33], v[196:203], v[134:137]
	v_mfma_f32_16x16x128_f8f6f4 v[118:121], v[18:25], v[204:211], v[118:121]
	v_mfma_f32_16x16x128_f8f6f4 v[110:113], v[26:33], v[204:211], v[110:113]
	s_setprio 0
	s_setprio 1
	v_mfma_f32_16x16x128_f8f6f4 v[138:141], v[2:9], v[174:181], v[138:141]
	v_mfma_f32_16x16x128_f8f6f4 v[130:133], v[10:17], v[174:181], v[130:133]
	v_mfma_f32_16x16x128_f8f6f4 v[126:129], v[2:9], v[188:195], v[126:129]
	v_mfma_f32_16x16x128_f8f6f4 v[122:125], v[10:17], v[188:195], v[122:125]
	v_mfma_f32_16x16x128_f8f6f4 v[114:117], v[2:9], v[196:203], v[114:117]
	v_mfma_f32_16x16x128_f8f6f4 v[106:109], v[10:17], v[196:203], v[106:109]
	v_mfma_f32_16x16x128_f8f6f4 v[102:105], v[2:9], v[204:211], v[102:105]
	v_mfma_f32_16x16x128_f8f6f4 v[98:101], v[10:17], v[204:211], v[98:101]
	s_setprio 0
	s_barrier
	s_add_i32 s41, s80, s56
	v_lshl_add_u64 v[174:175], s[46:47], 0, v[164:165]
	s_mov_b32 m0, s41
	ds_read_b128 v[188:191], v187 offset:16384
	ds_read_b128 v[192:195], v187 offset:17408
	ds_read_b128 v[196:199], v187 offset:18432
	ds_read_b128 v[200:203], v187 offset:19456
	ds_read_b128 v[204:207], v187 offset:20480
	ds_read_b128 v[208:211], v187 offset:21504
	ds_read_b128 v[212:215], v187 offset:22528
	ds_read_b128 v[216:219], v187 offset:23552
	global_load_lds_dwordx4 v[174:175], off
	s_add_i32 m0, s41, 0x2000
	s_add_u32 s50, s46, 0x40000
	v_lshl_add_u64 v[176:177], s[46:47], 0, v[162:163]
	s_addc_u32 s51, s47, 0
	s_add_i32 s41, s81, s56
	global_load_lds_dwordx4 v[176:177], off
	v_lshl_add_u64 v[178:179], s[50:51], 0, v[164:165]
	s_mov_b32 m0, s41
	v_lshl_add_u64 v[180:181], s[48:49], 0, v[168:169]
	global_load_lds_dwordx4 v[178:179], off
	v_lshl_add_u64 v[178:179], s[50:51], 0, v[162:163]
	s_add_i32 m0, s41, 0x2000
	s_nop 0
	global_load_lds_dwordx4 v[178:179], off
	v_lshl_add_u64 v[178:179], s[48:49], 0, v[166:167]
	s_mov_b32 m0, s1
	s_nop 0
	global_load_lds_dwordx4 v[178:179], off
	s_mov_b32 m0, s33
	s_nop 0
	global_load_lds_dwordx4 v[180:181], off
	s_waitcnt vmcnt(9)
	s_waitcnt lgkmcnt(0)
	s_barrier
	s_setprio 1
	s_waitcnt lgkmcnt(0)
	v_mfma_f32_16x16x128_f8f6f4 v[94:97], v[18:25], v[188:195], v[94:97]
	v_mfma_f32_16x16x128_f8f6f4 v[90:93], v[26:33], v[188:195], v[90:93]
	v_mfma_f32_16x16x128_f8f6f4 v[78:81], v[18:25], v[196:203], v[78:81]
	v_mfma_f32_16x16x128_f8f6f4 v[66:69], v[26:33], v[196:203], v[66:69]
	v_mfma_f32_16x16x128_f8f6f4 v[50:53], v[18:25], v[204:211], v[50:53]
	v_mfma_f32_16x16x128_f8f6f4 v[46:49], v[26:33], v[204:211], v[46:49]
	v_mfma_f32_16x16x128_f8f6f4 v[38:41], v[18:25], v[212:219], v[38:41]
	v_mfma_f32_16x16x128_f8f6f4 v[34:37], v[26:33], v[212:219], v[34:37]
	s_setprio 0
	s_setprio 1
	v_mfma_f32_16x16x128_f8f6f4 v[82:85], v[2:9], v[188:195], v[82:85]
	v_mfma_f32_16x16x128_f8f6f4 v[70:73], v[10:17], v[188:195], v[70:73]
	v_mfma_f32_16x16x128_f8f6f4 v[54:57], v[2:9], v[196:203], v[54:57]
	v_mfma_f32_16x16x128_f8f6f4 v[42:45], v[10:17], v[196:203], v[42:45]
	v_mfma_f32_16x16x128_f8f6f4 v[74:77], v[2:9], v[204:211], v[74:77]
	v_mfma_f32_16x16x128_f8f6f4 v[86:89], v[10:17], v[204:211], v[86:89]
	v_mfma_f32_16x16x128_f8f6f4 v[58:61], v[2:9], v[212:219], v[58:61]
	v_mfma_f32_16x16x128_f8f6f4 v[62:65], v[10:17], v[212:219], v[62:65]
	s_setprio 0
	s_barrier
	s_add_i32 s41, 0, 0x18000
	s_add_i32 s50, 0, 0x1c000
	v_add_u32_e32 v14, s41, v182
	v_add_u32_e32 v30, 0x1000, v14
	ds_read_b128 v[2:5], v14
	ds_read_b128 v[6:9], v14 offset:1024
	ds_read_b128 v[10:13], v14 offset:2048
	ds_read_b128 v[14:17], v14 offset:3072
	ds_read_b128 v[18:21], v30
	ds_read_b128 v[22:25], v30 offset:1024
	ds_read_b128 v[26:29], v30 offset:2048
	ds_read_b128 v[30:33], v30 offset:3072
	s_mov_b32 m0, s54
	v_lshl_add_u64 v[220:221], s[48:49], 0, v[170:171]
	ds_read_b128 v[188:191], v187 offset:32768
	ds_read_b128 v[192:195], v187 offset:33792
	ds_read_b128 v[196:199], v187 offset:34816
	ds_read_b128 v[200:203], v187 offset:35840
	ds_read_b128 v[204:207], v187 offset:36864
	ds_read_b128 v[208:211], v187 offset:37888
	ds_read_b128 v[212:215], v187 offset:38912
	ds_read_b128 v[216:219], v187 offset:39936
	global_load_lds_dwordx4 v[220:221], off
	v_lshl_add_u64 v[220:221], s[48:49], 0, v[172:173]
	s_mov_b32 m0, s57
	s_nop 0
	global_load_lds_dwordx4 v[220:221], off
	s_waitcnt vmcnt(9)
	s_waitcnt lgkmcnt(0)
	s_barrier
	s_setprio 1
	s_waitcnt lgkmcnt(0)
	v_mfma_f32_16x16x128_f8f6f4 v[158:161], v[2:9], v[188:195], v[158:161]
	v_mfma_f32_16x16x128_f8f6f4 v[154:157], v[10:17], v[188:195], v[154:157]
	v_mfma_f32_16x16x128_f8f6f4 v[150:153], v[2:9], v[196:203], v[150:153]
	v_mfma_f32_16x16x128_f8f6f4 v[146:149], v[10:17], v[196:203], v[146:149]
	v_mfma_f32_16x16x128_f8f6f4 v[142:145], v[2:9], v[204:211], v[142:145]
	v_mfma_f32_16x16x128_f8f6f4 v[134:137], v[10:17], v[204:211], v[134:137]
	v_mfma_f32_16x16x128_f8f6f4 v[118:121], v[2:9], v[212:219], v[118:121]
	v_mfma_f32_16x16x128_f8f6f4 v[110:113], v[10:17], v[212:219], v[110:113]
	s_setprio 0
	s_setprio 1
	v_mfma_f32_16x16x128_f8f6f4 v[138:141], v[18:25], v[188:195], v[138:141]
	v_mfma_f32_16x16x128_f8f6f4 v[130:133], v[26:33], v[188:195], v[130:133]
	v_mfma_f32_16x16x128_f8f6f4 v[126:129], v[18:25], v[196:203], v[126:129]
	v_mfma_f32_16x16x128_f8f6f4 v[122:125], v[26:33], v[196:203], v[122:125]
	v_mfma_f32_16x16x128_f8f6f4 v[114:117], v[18:25], v[204:211], v[114:117]
	v_mfma_f32_16x16x128_f8f6f4 v[106:109], v[26:33], v[204:211], v[106:109]
	v_mfma_f32_16x16x128_f8f6f4 v[102:105], v[18:25], v[212:219], v[102:105]
	v_mfma_f32_16x16x128_f8f6f4 v[98:101], v[26:33], v[212:219], v[98:101]
	s_setprio 0
	s_barrier
	s_add_i32 s41, s41, s56
	v_lshl_add_u64 v[174:175], v[174:175], 0, s[20:21]
	s_mov_b32 m0, s41
	ds_read_b128 v[188:191], v187 offset:49152
	ds_read_b128 v[192:195], v187 offset:50176
	ds_read_b128 v[196:199], v187 offset:51200
	ds_read_b128 v[200:203], v187 offset:52224
	ds_read_b128 v[204:207], v187 offset:53248
	ds_read_b128 v[208:211], v187 offset:54272
	ds_read_b128 v[212:215], v187 offset:55296
	ds_read_b128 v[216:219], v187 offset:56320
	global_load_lds_dwordx4 v[174:175], off
	s_add_i32 m0, s41, 0x2000
	s_add_u32 s46, s46, 0x40080
	v_lshl_add_u64 v[174:175], v[176:177], 0, s[20:21]
	s_addc_u32 s47, s47, 0
	s_add_i32 s41, s50, s56
	global_load_lds_dwordx4 v[174:175], off
	v_lshl_add_u64 v[174:175], s[46:47], 0, v[164:165]
	s_mov_b32 m0, s41
	s_nop 0
	global_load_lds_dwordx4 v[174:175], off
	v_lshl_add_u64 v[174:175], s[46:47], 0, v[162:163]
	s_add_i32 m0, s41, 0x2000
	s_nop 0
	global_load_lds_dwordx4 v[174:175], off
	v_lshl_add_u64 v[174:175], v[178:179], 0, s[20:21]
	s_mov_b32 m0, s60
	s_nop 0
	global_load_lds_dwordx4 v[174:175], off
	v_lshl_add_u64 v[174:175], v[180:181], 0, s[20:21]
	s_mov_b32 m0, s61
	s_nop 0
	global_load_lds_dwordx4 v[174:175], off
	s_waitcnt vmcnt(8)
	s_waitcnt lgkmcnt(0)
	s_barrier
	s_setprio 1
	s_waitcnt lgkmcnt(0)
	v_mfma_f32_16x16x128_f8f6f4 v[94:97], v[2:9], v[188:195], v[94:97]
	v_mfma_f32_16x16x128_f8f6f4 v[90:93], v[10:17], v[188:195], v[90:93]
	v_mfma_f32_16x16x128_f8f6f4 v[78:81], v[2:9], v[196:203], v[78:81]
	v_mfma_f32_16x16x128_f8f6f4 v[66:69], v[10:17], v[196:203], v[66:69]
	v_mfma_f32_16x16x128_f8f6f4 v[50:53], v[2:9], v[204:211], v[50:53]
	v_mfma_f32_16x16x128_f8f6f4 v[46:49], v[10:17], v[204:211], v[46:49]
	v_mfma_f32_16x16x128_f8f6f4 v[38:41], v[2:9], v[212:219], v[38:41]
	v_mfma_f32_16x16x128_f8f6f4 v[34:37], v[10:17], v[212:219], v[34:37]
	s_setprio 0
	s_setprio 1
	v_mfma_f32_16x16x128_f8f6f4 v[82:85], v[18:25], v[188:195], v[82:85]
	v_mfma_f32_16x16x128_f8f6f4 v[70:73], v[26:33], v[188:195], v[70:73]
	v_mfma_f32_16x16x128_f8f6f4 v[54:57], v[18:25], v[196:203], v[54:57]
	v_mfma_f32_16x16x128_f8f6f4 v[42:45], v[26:33], v[196:203], v[42:45]
	v_mfma_f32_16x16x128_f8f6f4 v[74:77], v[18:25], v[204:211], v[74:77]
	v_mfma_f32_16x16x128_f8f6f4 v[86:89], v[26:33], v[204:211], v[86:89]
	v_mfma_f32_16x16x128_f8f6f4 v[58:61], v[18:25], v[212:219], v[58:61]
	v_mfma_f32_16x16x128_f8f6f4 v[62:65], v[26:33], v[212:219], v[62:65]
	s_setprio 0
	s_barrier
	s_add_i32 s37, s37, 2
	s_cmp_gt_u32 s37, 13
	s_cbranch_scc0 .LBB0_1440
	s_and_b64 vcc, exec, s[22:23]
	s_cbranch_vccz .LBB0_1443
	s_barrier
.LBB0_1443:
	s_mov_b32 s100, s85
	s_mov_b32 s101, 0
	s_lshl_b64 s[100:101], s[100:101], 19
	s_add_u32 s100, s100, s18
	s_addc_u32 s101, s101, s19
	s_lshl_b32 vcc_lo, s10, 8
	s_add_u32 s100, s100, vcc_lo
	s_addc_u32 s101, s101, 0
	s_ashr_i32 s41, s40, 31
	s_lshl_b64 s[40:41], s[40:41], 13
	v_lshl_or_b32 v20, s10, 8, v183
	s_add_u32 s40, s12, s40
	s_addc_u32 s41, s13, s41
	v_ashrrev_i32_e32 v21, 31, v20
	v_lshl_add_u64 v[2:3], v[20:21], 2, s[40:41]
	global_load_dwordx4 v[14:17], v[2:3], off
	global_load_dwordx4 v[10:13], v[2:3], off offset:16
	global_load_dwordx4 v[6:9], v[2:3], off offset:128
	s_nop 0
	global_load_dwordx4 v[2:5], v[2:3], off offset:144
	v_mov_b32_e32 v24, 0
	v_mov_b32_e32 v25, 0
	v_mov_b32_e32 v26, 0
	v_mov_b32_e32 v27, 0
	v_mov_b32_e32 v28, 0
	v_mov_b32_e32 v29, 0
	v_mov_b32_e32 v30, 0
	v_mov_b32_e32 v31, 0
	v_lshl_add_u32 v18, s85, 8, v1
	v_mov_b32_e32 v174, 0
	v_mov_b32_e32 v175, 0
	v_ashrrev_i32_e32 v19, 31, v18
	v_or_b32_e32 v22, 16, v18
	v_or_b32_e32 v176, 32, v18
	v_or_b32_e32 v178, 48, v18
	v_lshlrev_b64 v[18:19], 11, v[18:19]
	v_ashrrev_i32_e32 v23, 31, v22
	v_lshl_add_u64 v[18:19], s[18:19], 0, v[18:19]
	v_lshlrev_b64 v[22:23], 11, v[22:23]
	v_lshl_add_u64 v[18:19], v[18:19], 0, v[20:21]
	v_lshl_add_u64 v[22:23], s[18:19], 0, v[22:23]
	v_lshl_add_u64 v[180:181], v[22:23], 0, v[20:21]
	v_mov_b32_e32 v32, 0
	v_mov_b32_e32 v33, 0
	v_ashrrev_i32_e32 v177, 31, v176
	v_ashrrev_i32_e32 v179, 31, v178
	v_lshlrev_b64 v[176:177], 11, v[176:177]
	v_lshlrev_b64 v[178:179], 11, v[178:179]
	v_lshl_add_u64 v[176:177], s[18:19], 0, v[176:177]
	v_lshl_add_u64 v[178:179], s[18:19], 0, v[178:179]
	v_lshl_add_u64 v[176:177], v[176:177], 0, v[20:21]
	v_lshl_add_u64 v[178:179], v[178:179], 0, v[20:21]
	v_lshl_add_u64 v[188:189], v[18:19], 0, s[14:15]
	v_lshl_add_u64 v[190:191], v[18:19], 0, s[24:25]
	v_lshl_add_u64 v[22:23], v[18:19], 0, s[26:27]
	v_lshl_add_u64 v[20:21], v[18:19], 0, s[28:29]
	s_waitcnt vmcnt(0)
	v_pk_fma_f32 v[158:159], v[158:159], s[30:31], v[14:15] op_sel_hi:[1,0,1]
	v_pk_fma_f32 v[154:155], v[154:155], s[30:31], v[10:11] op_sel_hi:[1,0,1]
	v_pk_fma_f32 v[138:139], v[138:139], s[30:31], v[6:7] op_sel_hi:[1,0,1]
	v_pk_fma_f32 v[130:131], v[130:131], s[30:31], v[2:3] op_sel_hi:[1,0,1]
	v_cvt_pk_fp8_f32 v24, v158, v159
	v_cvt_pk_fp8_f32 v25, v154, v155
	v_pk_fma_f32 v[150:151], v[150:151], s[30:31], v[14:15] op_sel_hi:[1,0,1]
	v_pk_fma_f32 v[146:147], v[146:147], s[30:31], v[10:11] op_sel_hi:[1,0,1]
	v_cvt_pk_fp8_f32 v26, v138, v139
	v_cvt_pk_fp8_f32 v27, v130, v131
	v_pk_fma_f32 v[126:127], v[126:127], s[30:31], v[6:7] op_sel_hi:[1,0,1]
	v_pk_fma_f32 v[122:123], v[122:123], s[30:31], v[2:3] op_sel_hi:[1,0,1]
	v_cvt_pk_fp8_f32 v28, v150, v151
	v_cvt_pk_fp8_f32 v29, v146, v147
	v_pk_fma_f32 v[160:161], v[160:161], s[30:31], v[16:17] op_sel_hi:[1,0,1]
	v_pk_fma_f32 v[156:157], v[156:157], s[30:31], v[12:13] op_sel_hi:[1,0,1]
	v_cvt_pk_fp8_f32 v30, v126, v127
	v_cvt_pk_fp8_f32 v31, v122, v123
	v_pk_fma_f32 v[140:141], v[140:141], s[30:31], v[8:9] op_sel_hi:[1,0,1]
	v_pk_fma_f32 v[132:133], v[132:133], s[30:31], v[4:5] op_sel_hi:[1,0,1]
	v_pk_fma_f32 v[114:115], v[114:115], s[30:31], v[6:7] op_sel_hi:[1,0,1]
	v_pk_fma_f32 v[106:107], v[106:107], s[30:31], v[2:3] op_sel_hi:[1,0,1]
	v_cvt_pk_fp8_f32 v24, v160, v161 op_sel:[0,0,1]
	v_cvt_pk_fp8_f32 v25, v156, v157 op_sel:[0,0,1]
	v_pk_fma_f32 v[152:153], v[152:153], s[30:31], v[16:17] op_sel_hi:[1,0,1]
	v_pk_fma_f32 v[148:149], v[148:149], s[30:31], v[12:13] op_sel_hi:[1,0,1]
	v_cvt_pk_fp8_f32 v174, v114, v115
	v_cvt_pk_fp8_f32 v26, v140, v141 op_sel:[0,0,1]
	v_cvt_pk_fp8_f32 v27, v132, v133 op_sel:[0,0,1]
	v_cvt_pk_fp8_f32 v175, v106, v107
	v_pk_fma_f32 v[128:129], v[128:129], s[30:31], v[8:9] op_sel_hi:[1,0,1]
	v_pk_fma_f32 v[124:125], v[124:125], s[30:31], v[4:5] op_sel_hi:[1,0,1]
	v_cvt_pk_fp8_f32 v28, v152, v153 op_sel:[0,0,1]
	v_cvt_pk_fp8_f32 v29, v148, v149 op_sel:[0,0,1]
	v_cvt_pk_fp8_f32 v30, v128, v129 op_sel:[0,0,1]
	v_cvt_pk_fp8_f32 v31, v124, v125 op_sel:[0,0,1]
	v_mov_b32_e32 v222, v24
	v_mov_b32_e32 v223, v25
	v_mov_b32_e32 v224, v26
	v_mov_b32_e32 v225, v27
	s_nop 1
	v_permlane16_swap_b32 v222, v224
	v_permlane16_swap_b32 v223, v225
	v_mov_b32_e32 v226, v28
	v_mov_b32_e32 v227, v29
	v_mov_b32_e32 v228, v30
	v_mov_b32_e32 v229, v31
	s_nop 1
	v_permlane16_swap_b32 v226, v228
	v_permlane16_swap_b32 v227, v229
	v_pk_fma_f32 v[24:25], v[116:117], s[30:31], v[8:9] op_sel_hi:[1,0,1]
	v_pk_fma_f32 v[26:27], v[108:109], s[30:31], v[4:5] op_sel_hi:[1,0,1]
	v_cvt_pk_fp8_f32 v174, v24, v25 op_sel:[0,0,1]
	v_cvt_pk_fp8_f32 v175, v26, v27 op_sel:[0,0,1]
	v_pk_fma_f32 v[24:25], v[118:119], s[30:31], v[14:15] op_sel_hi:[1,0,1]
	v_pk_fma_f32 v[26:27], v[110:111], s[30:31], v[10:11] op_sel_hi:[1,0,1]
	v_mov_b32_e32 v28, 0
	v_mov_b32_e32 v29, 0
	v_cvt_pk_fp8_f32 v28, v24, v25
	v_cvt_pk_fp8_f32 v29, v26, v27
	v_pk_fma_f32 v[142:143], v[142:143], s[30:31], v[14:15] op_sel_hi:[1,0,1]
	v_pk_fma_f32 v[134:135], v[134:135], s[30:31], v[10:11] op_sel_hi:[1,0,1]
	v_cvt_pk_fp8_f32 v32, v142, v143
	v_cvt_pk_fp8_f32 v33, v134, v135
	v_pk_fma_f32 v[24:25], v[120:121], s[30:31], v[16:17] op_sel_hi:[1,0,1]
	v_pk_fma_f32 v[26:27], v[112:113], s[30:31], v[12:13] op_sel_hi:[1,0,1]
	v_cvt_pk_fp8_f32 v28, v24, v25 op_sel:[0,0,1]
	v_cvt_pk_fp8_f32 v29, v26, v27 op_sel:[0,0,1]
	v_pk_fma_f32 v[24:25], v[102:103], s[30:31], v[6:7] op_sel_hi:[1,0,1]
	v_pk_fma_f32 v[26:27], v[98:99], s[30:31], v[2:3] op_sel_hi:[1,0,1]
	v_mov_b32_e32 v30, 0
	v_mov_b32_e32 v31, 0
	v_pk_fma_f32 v[144:145], v[144:145], s[30:31], v[16:17] op_sel_hi:[1,0,1]
	v_pk_fma_f32 v[136:137], v[136:137], s[30:31], v[12:13] op_sel_hi:[1,0,1]
	v_cvt_pk_fp8_f32 v30, v24, v25
	v_cvt_pk_fp8_f32 v31, v26, v27
	v_cvt_pk_fp8_f32 v32, v144, v145 op_sel:[0,0,1]
	v_cvt_pk_fp8_f32 v33, v136, v137 op_sel:[0,0,1]
	v_pk_fma_f32 v[24:25], v[104:105], s[30:31], v[8:9] op_sel_hi:[1,0,1]
	v_pk_fma_f32 v[26:27], v[100:101], s[30:31], v[4:5] op_sel_hi:[1,0,1]
	v_cvt_pk_fp8_f32 v30, v24, v25 op_sel:[0,0,1]
	v_cvt_pk_fp8_f32 v31, v26, v27 op_sel:[0,0,1]
	v_mov_b32_e32 v230, v32
	v_mov_b32_e32 v231, v33
	v_mov_b32_e32 v232, v174
	v_mov_b32_e32 v233, v175
	s_nop 1
	v_permlane16_swap_b32 v230, v232
	v_permlane16_swap_b32 v231, v233
	v_mov_b32_e32 v234, v28
	v_mov_b32_e32 v235, v29
	v_mov_b32_e32 v236, v30
	v_mov_b32_e32 v237, v31
	s_nop 1
	v_permlane16_swap_b32 v234, v236
	v_permlane16_swap_b32 v235, v237
	v_pk_fma_f32 v[24:25], v[94:95], s[30:31], v[14:15] op_sel_hi:[1,0,1]
	v_pk_fma_f32 v[26:27], v[90:91], s[30:31], v[10:11] op_sel_hi:[1,0,1]
	v_mov_b32_e32 v28, 0
	v_mov_b32_e32 v29, 0
	v_cvt_pk_fp8_f32 v28, v24, v25
	v_cvt_pk_fp8_f32 v29, v26, v27
	v_pk_fma_f32 v[24:25], v[96:97], s[30:31], v[16:17] op_sel_hi:[1,0,1]
	v_pk_fma_f32 v[26:27], v[92:93], s[30:31], v[12:13] op_sel_hi:[1,0,1]
	v_cvt_pk_fp8_f32 v28, v24, v25 op_sel:[0,0,1]
	v_cvt_pk_fp8_f32 v29, v26, v27 op_sel:[0,0,1]
	v_pk_fma_f32 v[24:25], v[82:83], s[30:31], v[6:7] op_sel_hi:[1,0,1]
	v_pk_fma_f32 v[26:27], v[70:71], s[30:31], v[2:3] op_sel_hi:[1,0,1]
	v_mov_b32_e32 v30, 0
	v_mov_b32_e32 v31, 0
	v_cvt_pk_fp8_f32 v30, v24, v25
	v_cvt_pk_fp8_f32 v31, v26, v27
	v_pk_fma_f32 v[24:25], v[84:85], s[30:31], v[8:9] op_sel_hi:[1,0,1]
	v_pk_fma_f32 v[26:27], v[72:73], s[30:31], v[4:5] op_sel_hi:[1,0,1]
	v_cvt_pk_fp8_f32 v30, v24, v25 op_sel:[0,0,1]
	v_cvt_pk_fp8_f32 v31, v26, v27 op_sel:[0,0,1]
	v_add_co_u32_e32 v24, vcc, s58, v18
	v_pk_fma_f32 v[26:27], v[66:67], s[30:31], v[10:11] op_sel_hi:[1,0,1]
	s_nop 0
	v_addc_co_u32_e32 v25, vcc, 0, v19, vcc
	v_mov_b32_e32 v238, v28
	v_mov_b32_e32 v239, v29
	v_mov_b32_e32 v240, v30
	v_mov_b32_e32 v241, v31
	s_nop 1
	v_permlane16_swap_b32 v238, v240
	v_permlane16_swap_b32 v239, v241
	v_pk_fma_f32 v[24:25], v[78:79], s[30:31], v[14:15] op_sel_hi:[1,0,1]
	v_mov_b32_e32 v28, 0
	v_mov_b32_e32 v29, 0
	v_cvt_pk_fp8_f32 v28, v24, v25
	v_cvt_pk_fp8_f32 v29, v26, v27
	v_pk_fma_f32 v[24:25], v[80:81], s[30:31], v[16:17] op_sel_hi:[1,0,1]
	v_pk_fma_f32 v[26:27], v[68:69], s[30:31], v[12:13] op_sel_hi:[1,0,1]
	v_cvt_pk_fp8_f32 v28, v24, v25 op_sel:[0,0,1]
	v_cvt_pk_fp8_f32 v29, v26, v27 op_sel:[0,0,1]
	v_pk_fma_f32 v[24:25], v[54:55], s[30:31], v[6:7] op_sel_hi:[1,0,1]
	v_pk_fma_f32 v[26:27], v[42:43], s[30:31], v[2:3] op_sel_hi:[1,0,1]
	v_mov_b32_e32 v30, 0
	v_mov_b32_e32 v31, 0
	v_cvt_pk_fp8_f32 v30, v24, v25
	v_cvt_pk_fp8_f32 v31, v26, v27
	v_pk_fma_f32 v[24:25], v[56:57], s[30:31], v[8:9] op_sel_hi:[1,0,1]
	v_pk_fma_f32 v[26:27], v[44:45], s[30:31], v[4:5] op_sel_hi:[1,0,1]
	v_cvt_pk_fp8_f32 v30, v24, v25 op_sel:[0,0,1]
	v_cvt_pk_fp8_f32 v31, v26, v27 op_sel:[0,0,1]
	v_add_co_u32_e32 v24, vcc, s82, v18
	v_pk_fma_f32 v[26:27], v[46:47], s[30:31], v[10:11] op_sel_hi:[1,0,1]
	s_nop 0
	v_addc_co_u32_e32 v25, vcc, 0, v19, vcc
	v_mov_b32_e32 v242, v28
	v_mov_b32_e32 v243, v29
	v_mov_b32_e32 v244, v30
	v_mov_b32_e32 v245, v31
	s_nop 1
	v_permlane16_swap_b32 v242, v244
	v_permlane16_swap_b32 v243, v245
	v_pk_fma_f32 v[24:25], v[50:51], s[30:31], v[14:15] op_sel_hi:[1,0,1]
	v_mov_b32_e32 v28, 0
	v_mov_b32_e32 v29, 0
	v_cvt_pk_fp8_f32 v28, v24, v25
	v_cvt_pk_fp8_f32 v29, v26, v27
	v_pk_fma_f32 v[24:25], v[52:53], s[30:31], v[16:17] op_sel_hi:[1,0,1]
	v_pk_fma_f32 v[26:27], v[48:49], s[30:31], v[12:13] op_sel_hi:[1,0,1]
	v_cvt_pk_fp8_f32 v28, v24, v25 op_sel:[0,0,1]
	v_cvt_pk_fp8_f32 v29, v26, v27 op_sel:[0,0,1]
	v_pk_fma_f32 v[24:25], v[74:75], s[30:31], v[6:7] op_sel_hi:[1,0,1]
	v_pk_fma_f32 v[26:27], v[86:87], s[30:31], v[2:3] op_sel_hi:[1,0,1]
	v_mov_b32_e32 v30, 0
	v_mov_b32_e32 v31, 0
	v_cvt_pk_fp8_f32 v30, v24, v25
	v_cvt_pk_fp8_f32 v31, v26, v27
	v_pk_fma_f32 v[24:25], v[76:77], s[30:31], v[8:9] op_sel_hi:[1,0,1]
	v_pk_fma_f32 v[26:27], v[88:89], s[30:31], v[4:5] op_sel_hi:[1,0,1]
	v_cvt_pk_fp8_f32 v30, v24, v25 op_sel:[0,0,1]
	v_cvt_pk_fp8_f32 v31, v26, v27 op_sel:[0,0,1]
	v_add_co_u32_e32 v24, vcc, s83, v18
	v_pk_fma_f32 v[14:15], v[38:39], s[30:31], v[14:15] op_sel_hi:[1,0,1]
	s_nop 0
	v_addc_co_u32_e32 v25, vcc, 0, v19, vcc
	v_mov_b32_e32 v246, v28
	v_mov_b32_e32 v247, v29
	v_mov_b32_e32 v248, v30
	v_mov_b32_e32 v249, v31
	s_nop 1
	v_permlane16_swap_b32 v246, v248
	v_permlane16_swap_b32 v247, v249
	v_mov_b32_e32 v22, 0
	v_cvt_pk_fp8_f32 v22, v14, v15
	v_pk_fma_f32 v[10:11], v[34:35], s[30:31], v[10:11] op_sel_hi:[1,0,1]
	v_mov_b32_e32 v23, 0
	v_cvt_pk_fp8_f32 v23, v10, v11
	v_pk_fma_f32 v[10:11], v[40:41], s[30:31], v[16:17] op_sel_hi:[1,0,1]
	v_pk_fma_f32 v[6:7], v[58:59], s[30:31], v[6:7] op_sel_hi:[1,0,1]
	v_cvt_pk_fp8_f32 v22, v10, v11 op_sel:[0,0,1]
	v_pk_fma_f32 v[2:3], v[62:63], s[30:31], v[2:3] op_sel_hi:[1,0,1]
	v_mov_b32_e32 v10, 0
	v_mov_b32_e32 v11, 0
	v_cvt_pk_fp8_f32 v10, v6, v7
	v_cvt_pk_fp8_f32 v11, v2, v3
	v_pk_fma_f32 v[12:13], v[36:37], s[30:31], v[12:13] op_sel_hi:[1,0,1]
	v_pk_fma_f32 v[2:3], v[60:61], s[30:31], v[8:9] op_sel_hi:[1,0,1]
	v_cvt_pk_fp8_f32 v23, v12, v13 op_sel:[0,0,1]
	v_pk_fma_f32 v[4:5], v[64:65], s[30:31], v[4:5] op_sel_hi:[1,0,1]
	v_cvt_pk_fp8_f32 v10, v2, v3 op_sel:[0,0,1]
	v_cvt_pk_fp8_f32 v11, v4, v5 op_sel:[0,0,1]
	v_add_co_u32_e32 v2, vcc, s84, v18
	s_nop 1
	v_addc_co_u32_e32 v3, vcc, 0, v19, vcc
	s_andn2_b64 vcc, exec, s[6:7]
	s_mov_b64 s[6:7], -1
	v_mov_b32_e32 v250, v22
	v_mov_b32_e32 v251, v23
	v_mov_b32_e32 v252, v10
	v_mov_b32_e32 v253, v11
	s_nop 1
	v_permlane16_swap_b32 v250, v252
	v_permlane16_swap_b32 v251, v253
	s_cbranch_vccnz .LBB0_1434
	s_andn2_b64 vcc, exec, s[16:17]
	s_cbranch_vccnz .LBB0_1433
	s_barrier
	s_branch .LBB0_1433

.LBB0_1448:
	global_store_dwordx4 v1, v[222:225], s[100:101]
	s_add_u32 s100, s100, 0x8000
	s_addc_u32 s101, s101, 0
	global_store_dwordx4 v1, v[226:229], s[100:101]
	s_add_u32 s100, s100, 0x8000
	s_addc_u32 s101, s101, 0
	global_store_dwordx4 v1, v[230:233], s[100:101]
	s_add_u32 s100, s100, 0x8000
	s_addc_u32 s101, s101, 0
	global_store_dwordx4 v1, v[234:237], s[100:101]
	s_add_u32 s100, s100, 0x28000
	s_addc_u32 s101, s101, 0
	global_store_dwordx4 v1, v[238:241], s[100:101]
	s_add_u32 s100, s100, 0x8000
	s_addc_u32 s101, s101, 0
	global_store_dwordx4 v1, v[242:245], s[100:101]
	s_add_u32 s100, s100, 0x8000
	s_addc_u32 s101, s101, 0
	global_store_dwordx4 v1, v[246:249], s[100:101]
	s_add_u32 s100, s100, 0x8000
	s_addc_u32 s101, s101, 0
	global_store_dwordx4 v1, v[250:253], s[100:101]
	s_waitcnt vmcnt(0)
	v_readlane_b32 s76, v255, 20
	v_readlane_b32 s77, v255, 21
	s_barrier
